# v23 + moe-down gate loads hoisted from the epilogue start to the start of the unit's tail K step (counted wait in the epilogue)
# speedup vs baseline: 1.0003x; 1.0003x over previous
.LBB0_1506:
	s_add_u32 s61, s22, s18
	s_addc_u32 s66, s23, s19
	v_add_u32_e32 v132, 0x10000, v142
	v_add_u32_e32 v133, 0x14000, v142
	s_add_u32 s34, s61, 0x100
	ds_read_b128 v[134:137], v132
	ds_read_b128 v[144:147], v132 offset:1024
	ds_read_b128 v[148:151], v132 offset:2048
	ds_read_b128 v[152:155], v132 offset:3072
	ds_read_b128 v[156:159], v133
	ds_read_b128 v[160:163], v133 offset:1024
	ds_read_b128 v[164:167], v133 offset:2048
	ds_read_b128 v[168:171], v133 offset:3072
	s_addc_u32 s35, s66, 0
	s_add_u32 s26, s61, 0x180
	s_addc_u32 s27, s66, 0
	s_add_u32 s15, s24, s18
	s_addc_u32 s33, s25, s19
	s_add_u32 s62, s15, 0x100
	s_addc_u32 s63, s33, 0
	ds_read_b128 v[172:175], v143
	ds_read_b128 v[176:179], v143 offset:1024
	ds_read_b128 v[180:183], v143 offset:2048
	ds_read_b128 v[184:187], v143 offset:3072
	ds_read_b128 v[188:191], v143 offset:4096
	ds_read_b128 v[194:197], v143 offset:5120
	ds_read_b128 v[198:201], v143 offset:6144
	ds_read_b128 v[202:205], v143 offset:7168
	s_add_u32 s64, s61, 0x40080
	s_addc_u32 s65, s66, 0
	s_mov_b32 m0, s57
	s_nop 0
	global_load_lds_dwordx4 v65, s[64:65]
	s_nop 0
	s_mov_b32 m0, s58
	s_nop 0
	global_load_lds_dwordx4 v140, s[64:65]
	s_waitcnt vmcnt(8)
	s_waitcnt lgkmcnt(0)
	s_barrier
	s_setprio 1
	s_waitcnt lgkmcnt(0)
	v_mfma_f32_16x16x32_bf16 v[128:131], v[134:137], v[172:175], v[128:131]
	v_mfma_f32_16x16x32_bf16 v[124:127], v[148:151], v[172:175], v[124:127]
	s_waitcnt lgkmcnt(5)
	v_mfma_f32_16x16x32_bf16 v[120:123], v[134:137], v[180:183], v[120:123]
	v_mfma_f32_16x16x32_bf16 v[116:119], v[148:151], v[180:183], v[116:119]
	s_waitcnt lgkmcnt(3)
	v_mfma_f32_16x16x32_bf16 v[110:113], v[134:137], v[188:191], v[110:113]
	v_mfma_f32_16x16x32_bf16 v[106:109], v[148:151], v[188:191], v[106:109]
	s_waitcnt lgkmcnt(1)
	v_mfma_f32_16x16x32_bf16 v[102:105], v[134:137], v[198:201], v[102:105]
	v_mfma_f32_16x16x32_bf16 v[98:101], v[148:151], v[198:201], v[98:101]
	v_mfma_f32_16x16x32_bf16 v[128:131], v[144:147], v[176:179], v[128:131]
	v_mfma_f32_16x16x32_bf16 v[124:127], v[152:155], v[176:179], v[124:127]
	v_mfma_f32_16x16x32_bf16 v[120:123], v[144:147], v[184:187], v[120:123]
	v_mfma_f32_16x16x32_bf16 v[116:119], v[152:155], v[184:187], v[116:119]
	v_mfma_f32_16x16x32_bf16 v[110:113], v[144:147], v[194:197], v[110:113]
	v_mfma_f32_16x16x32_bf16 v[106:109], v[152:155], v[194:197], v[106:109]
	s_waitcnt lgkmcnt(0)
	v_mfma_f32_16x16x32_bf16 v[102:105], v[144:147], v[202:205], v[102:105]
	v_mfma_f32_16x16x32_bf16 v[98:101], v[152:155], v[202:205], v[98:101]
	s_setprio 0
	s_setprio 1
	v_mfma_f32_16x16x32_bf16 v[94:97], v[156:159], v[172:175], v[94:97]
	v_mfma_f32_16x16x32_bf16 v[90:93], v[164:167], v[172:175], v[90:93]
	v_mfma_f32_16x16x32_bf16 v[86:89], v[156:159], v[180:183], v[86:89]
	v_mfma_f32_16x16x32_bf16 v[82:85], v[164:167], v[180:183], v[82:85]
	v_mfma_f32_16x16x32_bf16 v[78:81], v[156:159], v[188:191], v[78:81]
	v_mfma_f32_16x16x32_bf16 v[74:77], v[164:167], v[188:191], v[74:77]
	v_mfma_f32_16x16x32_bf16 v[70:73], v[156:159], v[198:201], v[70:73]
	v_mfma_f32_16x16x32_bf16 v[66:69], v[164:167], v[198:201], v[66:69]
	v_mfma_f32_16x16x32_bf16 v[94:97], v[160:163], v[176:179], v[94:97]
	v_mfma_f32_16x16x32_bf16 v[90:93], v[168:171], v[176:179], v[90:93]
	v_mfma_f32_16x16x32_bf16 v[86:89], v[160:163], v[184:187], v[86:89]
	v_mfma_f32_16x16x32_bf16 v[82:85], v[168:171], v[184:187], v[82:85]
	v_mfma_f32_16x16x32_bf16 v[78:81], v[160:163], v[194:197], v[78:81]
	v_mfma_f32_16x16x32_bf16 v[74:77], v[168:171], v[194:197], v[74:77]
	v_mfma_f32_16x16x32_bf16 v[70:73], v[160:163], v[202:205], v[70:73]
	v_mfma_f32_16x16x32_bf16 v[66:69], v[168:171], v[202:205], v[66:69]
	s_setprio 0
	s_barrier
	ds_read_b128 v[172:175], v143 offset:16384
	ds_read_b128 v[176:179], v143 offset:17408
	ds_read_b128 v[180:183], v143 offset:18432
	ds_read_b128 v[184:187], v143 offset:19456
	ds_read_b128 v[188:191], v143 offset:20480
	ds_read_b128 v[194:197], v143 offset:21504
	ds_read_b128 v[198:201], v143 offset:22528
	ds_read_b128 v[202:205], v143 offset:23552
	s_mov_b32 m0, s41
	s_nop 0
	global_load_lds_dwordx4 v114, s[62:63]
	s_nop 0
	s_mov_b32 m0, s42
	s_nop 0
	global_load_lds_dwordx4 v141, s[62:63]
	s_add_u32 s62, s15, 0x40100
	s_addc_u32 s63, s33, 0
	s_mov_b32 m0, s43
	s_nop 0
	global_load_lds_dwordx4 v114, s[62:63]
	s_nop 0
	s_mov_b32 m0, s44
	s_nop 0
	global_load_lds_dwordx4 v141, s[62:63]
	s_mov_b32 m0, s40
	s_nop 0
	global_load_lds_dwordx4 v65, s[34:35]
	s_nop 0
	s_mov_b32 m0, s45
	s_nop 0
	global_load_lds_dwordx4 v140, s[34:35]
	s_waitcnt vmcnt(8)
	s_waitcnt lgkmcnt(0)
	s_barrier
	s_setprio 1
	s_waitcnt lgkmcnt(0)
	v_mfma_f32_16x16x32_bf16 v[60:63], v[134:137], v[172:175], v[60:63]
	v_mfma_f32_16x16x32_bf16 v[56:59], v[148:151], v[172:175], v[56:59]
	s_waitcnt lgkmcnt(5)
	v_mfma_f32_16x16x32_bf16 v[52:55], v[134:137], v[180:183], v[52:55]
	v_mfma_f32_16x16x32_bf16 v[48:51], v[148:151], v[180:183], v[48:51]
	s_waitcnt lgkmcnt(3)
	v_mfma_f32_16x16x32_bf16 v[44:47], v[134:137], v[188:191], v[44:47]
	v_mfma_f32_16x16x32_bf16 v[40:43], v[148:151], v[188:191], v[40:43]
	s_waitcnt lgkmcnt(1)
	v_mfma_f32_16x16x32_bf16 v[36:39], v[134:137], v[198:201], v[36:39]
	v_mfma_f32_16x16x32_bf16 v[32:35], v[148:151], v[198:201], v[32:35]
	v_mfma_f32_16x16x32_bf16 v[60:63], v[144:147], v[176:179], v[60:63]
	v_mfma_f32_16x16x32_bf16 v[56:59], v[152:155], v[176:179], v[56:59]
	v_mfma_f32_16x16x32_bf16 v[52:55], v[144:147], v[184:187], v[52:55]
	v_mfma_f32_16x16x32_bf16 v[48:51], v[152:155], v[184:187], v[48:51]
	v_mfma_f32_16x16x32_bf16 v[44:47], v[144:147], v[194:197], v[44:47]
	v_mfma_f32_16x16x32_bf16 v[40:43], v[152:155], v[194:197], v[40:43]
	s_waitcnt lgkmcnt(0)
	v_mfma_f32_16x16x32_bf16 v[36:39], v[144:147], v[202:205], v[36:39]
	v_mfma_f32_16x16x32_bf16 v[32:35], v[152:155], v[202:205], v[32:35]
	s_setprio 0
	s_setprio 1
	v_mfma_f32_16x16x32_bf16 v[28:31], v[156:159], v[172:175], v[28:31]
	v_mfma_f32_16x16x32_bf16 v[24:27], v[164:167], v[172:175], v[24:27]
	v_mfma_f32_16x16x32_bf16 v[20:23], v[156:159], v[180:183], v[20:23]
	v_mfma_f32_16x16x32_bf16 v[16:19], v[164:167], v[180:183], v[16:19]
	v_mfma_f32_16x16x32_bf16 v[12:15], v[156:159], v[188:191], v[12:15]
	v_mfma_f32_16x16x32_bf16 v[8:11], v[164:167], v[188:191], v[8:11]
	v_mfma_f32_16x16x32_bf16 v[4:7], v[156:159], v[198:201], v[4:7]
	v_mfma_f32_16x16x32_bf16 v[0:3], v[164:167], v[198:201], v[0:3]
	v_mfma_f32_16x16x32_bf16 v[28:31], v[160:163], v[176:179], v[28:31]
	v_mfma_f32_16x16x32_bf16 v[24:27], v[168:171], v[176:179], v[24:27]
	v_mfma_f32_16x16x32_bf16 v[20:23], v[160:163], v[184:187], v[20:23]
	v_mfma_f32_16x16x32_bf16 v[16:19], v[168:171], v[184:187], v[16:19]
	v_mfma_f32_16x16x32_bf16 v[12:15], v[160:163], v[194:197], v[12:15]
	v_mfma_f32_16x16x32_bf16 v[8:11], v[168:171], v[194:197], v[8:11]
	v_mfma_f32_16x16x32_bf16 v[4:7], v[160:163], v[202:205], v[4:7]
	v_mfma_f32_16x16x32_bf16 v[0:3], v[168:171], v[202:205], v[0:3]
	s_setprio 0
	s_barrier
	v_add_u32_e32 v134, 0x18000, v142
	v_add_u32_e32 v135, 0x1c000, v142
	ds_read_b128 v[136:139], v134
	ds_read_b128 v[144:147], v134 offset:1024
	ds_read_b128 v[148:151], v134 offset:2048
	ds_read_b128 v[152:155], v134 offset:3072
	ds_read_b128 v[156:159], v135
	ds_read_b128 v[160:163], v135 offset:1024
	ds_read_b128 v[164:167], v135 offset:2048
	ds_read_b128 v[168:171], v135 offset:3072
	ds_read_b128 v[172:175], v143 offset:32768
	ds_read_b128 v[176:179], v143 offset:33792
	ds_read_b128 v[180:183], v143 offset:34816
	ds_read_b128 v[184:187], v143 offset:35840
	ds_read_b128 v[188:191], v143 offset:36864
	ds_read_b128 v[194:197], v143 offset:37888
	ds_read_b128 v[198:201], v143 offset:38912
	ds_read_b128 v[202:205], v143 offset:39936
	s_add_u32 s34, s61, 0x40100
	s_addc_u32 s35, s66, 0
	s_mov_b32 m0, s46
	s_nop 0
	global_load_lds_dwordx4 v65, s[34:35]
	s_nop 0
	s_mov_b32 m0, s47
	s_nop 0
	global_load_lds_dwordx4 v140, s[34:35]
	s_waitcnt vmcnt(8)
	s_waitcnt lgkmcnt(0)
	s_barrier
	s_setprio 1
	s_waitcnt lgkmcnt(0)
	v_mfma_f32_16x16x32_bf16 v[128:131], v[136:139], v[172:175], v[128:131]
	v_mfma_f32_16x16x32_bf16 v[124:127], v[148:151], v[172:175], v[124:127]
	s_waitcnt lgkmcnt(5)
	v_mfma_f32_16x16x32_bf16 v[120:123], v[136:139], v[180:183], v[120:123]
	v_mfma_f32_16x16x32_bf16 v[116:119], v[148:151], v[180:183], v[116:119]
	s_waitcnt lgkmcnt(3)
	v_mfma_f32_16x16x32_bf16 v[110:113], v[136:139], v[188:191], v[110:113]
	v_mfma_f32_16x16x32_bf16 v[106:109], v[148:151], v[188:191], v[106:109]
	s_waitcnt lgkmcnt(1)
	v_mfma_f32_16x16x32_bf16 v[102:105], v[136:139], v[198:201], v[102:105]
	v_mfma_f32_16x16x32_bf16 v[98:101], v[148:151], v[198:201], v[98:101]
	v_mfma_f32_16x16x32_bf16 v[128:131], v[144:147], v[176:179], v[128:131]
	v_mfma_f32_16x16x32_bf16 v[124:127], v[152:155], v[176:179], v[124:127]
	v_mfma_f32_16x16x32_bf16 v[120:123], v[144:147], v[184:187], v[120:123]
	v_mfma_f32_16x16x32_bf16 v[116:119], v[152:155], v[184:187], v[116:119]
	v_mfma_f32_16x16x32_bf16 v[110:113], v[144:147], v[194:197], v[110:113]
	v_mfma_f32_16x16x32_bf16 v[106:109], v[152:155], v[194:197], v[106:109]
	s_waitcnt lgkmcnt(0)
	v_mfma_f32_16x16x32_bf16 v[102:105], v[144:147], v[202:205], v[102:105]
	v_mfma_f32_16x16x32_bf16 v[98:101], v[152:155], v[202:205], v[98:101]
	s_setprio 0
	s_setprio 1
	v_mfma_f32_16x16x32_bf16 v[94:97], v[156:159], v[172:175], v[94:97]
	v_mfma_f32_16x16x32_bf16 v[90:93], v[164:167], v[172:175], v[90:93]
	v_mfma_f32_16x16x32_bf16 v[86:89], v[156:159], v[180:183], v[86:89]
	v_mfma_f32_16x16x32_bf16 v[82:85], v[164:167], v[180:183], v[82:85]
	v_mfma_f32_16x16x32_bf16 v[78:81], v[156:159], v[188:191], v[78:81]
	v_mfma_f32_16x16x32_bf16 v[74:77], v[164:167], v[188:191], v[74:77]
	v_mfma_f32_16x16x32_bf16 v[70:73], v[156:159], v[198:201], v[70:73]
	v_mfma_f32_16x16x32_bf16 v[66:69], v[164:167], v[198:201], v[66:69]
	v_mfma_f32_16x16x32_bf16 v[94:97], v[160:163], v[176:179], v[94:97]
	v_mfma_f32_16x16x32_bf16 v[90:93], v[168:171], v[176:179], v[90:93]
	v_mfma_f32_16x16x32_bf16 v[86:89], v[160:163], v[184:187], v[86:89]
	v_mfma_f32_16x16x32_bf16 v[82:85], v[168:171], v[184:187], v[82:85]
	v_mfma_f32_16x16x32_bf16 v[78:81], v[160:163], v[194:197], v[78:81]
	v_mfma_f32_16x16x32_bf16 v[74:77], v[168:171], v[194:197], v[74:77]
	v_mfma_f32_16x16x32_bf16 v[70:73], v[160:163], v[202:205], v[70:73]
	v_mfma_f32_16x16x32_bf16 v[66:69], v[168:171], v[202:205], v[66:69]
	s_setprio 0
	s_barrier
	ds_read_b128 v[172:175], v143 offset:49152
	ds_read_b128 v[176:179], v143 offset:50176
	ds_read_b128 v[180:183], v143 offset:51200
	ds_read_b128 v[184:187], v143 offset:52224
	ds_read_b128 v[188:191], v143 offset:53248
	ds_read_b128 v[194:197], v143 offset:54272
	ds_read_b128 v[198:201], v143 offset:55296
	ds_read_b128 v[202:205], v143 offset:56320
	s_add_u32 s34, s15, 0x180
	s_addc_u32 s35, s33, 0
	s_mov_b32 m0, s51
	s_nop 0
	global_load_lds_dwordx4 v114, s[34:35]
	s_nop 0
	s_mov_b32 m0, s52
	s_nop 0
	global_load_lds_dwordx4 v141, s[34:35]
	s_add_u32 s34, s15, 0x40180
	s_addc_u32 s35, s33, 0
	s_mov_b32 m0, s55
	s_nop 0
	global_load_lds_dwordx4 v114, s[34:35]
	s_nop 0
	s_mov_b32 m0, s56
	s_nop 0
	global_load_lds_dwordx4 v141, s[34:35]
	s_nop 0
	s_mov_b32 m0, s53
	s_nop 0
	global_load_lds_dwordx4 v65, s[26:27]
	s_nop 0
	s_mov_b32 m0, s54
	s_nop 0
	global_load_lds_dwordx4 v140, s[26:27]
	s_waitcnt vmcnt(8)
	s_waitcnt lgkmcnt(0)
	s_barrier
	s_setprio 1
	s_waitcnt lgkmcnt(0)
	v_mfma_f32_16x16x32_bf16 v[60:63], v[136:139], v[172:175], v[60:63]
	v_mfma_f32_16x16x32_bf16 v[56:59], v[148:151], v[172:175], v[56:59]
	s_waitcnt lgkmcnt(5)
	v_mfma_f32_16x16x32_bf16 v[52:55], v[136:139], v[180:183], v[52:55]
	v_mfma_f32_16x16x32_bf16 v[48:51], v[148:151], v[180:183], v[48:51]
	s_waitcnt lgkmcnt(3)
	v_mfma_f32_16x16x32_bf16 v[44:47], v[136:139], v[188:191], v[44:47]
	v_mfma_f32_16x16x32_bf16 v[40:43], v[148:151], v[188:191], v[40:43]
	s_waitcnt lgkmcnt(1)
	v_mfma_f32_16x16x32_bf16 v[36:39], v[136:139], v[198:201], v[36:39]
	v_mfma_f32_16x16x32_bf16 v[32:35], v[148:151], v[198:201], v[32:35]
	v_mfma_f32_16x16x32_bf16 v[60:63], v[144:147], v[176:179], v[60:63]
	v_mfma_f32_16x16x32_bf16 v[56:59], v[152:155], v[176:179], v[56:59]
	v_mfma_f32_16x16x32_bf16 v[52:55], v[144:147], v[184:187], v[52:55]
	v_mfma_f32_16x16x32_bf16 v[48:51], v[152:155], v[184:187], v[48:51]
	v_mfma_f32_16x16x32_bf16 v[44:47], v[144:147], v[194:197], v[44:47]
	v_mfma_f32_16x16x32_bf16 v[40:43], v[152:155], v[194:197], v[40:43]
	s_waitcnt lgkmcnt(0)
	v_mfma_f32_16x16x32_bf16 v[36:39], v[144:147], v[202:205], v[36:39]
	v_mfma_f32_16x16x32_bf16 v[32:35], v[152:155], v[202:205], v[32:35]
	s_setprio 0
	s_setprio 1
	v_mfma_f32_16x16x32_bf16 v[28:31], v[156:159], v[172:175], v[28:31]
	v_mfma_f32_16x16x32_bf16 v[24:27], v[164:167], v[172:175], v[24:27]
	v_mfma_f32_16x16x32_bf16 v[20:23], v[156:159], v[180:183], v[20:23]
	v_mfma_f32_16x16x32_bf16 v[16:19], v[164:167], v[180:183], v[16:19]
	v_mfma_f32_16x16x32_bf16 v[12:15], v[156:159], v[188:191], v[12:15]
	v_mfma_f32_16x16x32_bf16 v[8:11], v[164:167], v[188:191], v[8:11]
	v_mfma_f32_16x16x32_bf16 v[4:7], v[156:159], v[198:201], v[4:7]
	v_mfma_f32_16x16x32_bf16 v[0:3], v[164:167], v[198:201], v[0:3]
	v_mfma_f32_16x16x32_bf16 v[28:31], v[160:163], v[176:179], v[28:31]
	v_mfma_f32_16x16x32_bf16 v[24:27], v[168:171], v[176:179], v[24:27]
	v_mfma_f32_16x16x32_bf16 v[20:23], v[160:163], v[184:187], v[20:23]
	v_mfma_f32_16x16x32_bf16 v[16:19], v[168:171], v[184:187], v[16:19]
	v_mfma_f32_16x16x32_bf16 v[12:15], v[160:163], v[194:197], v[12:15]
	v_mfma_f32_16x16x32_bf16 v[8:11], v[168:171], v[194:197], v[8:11]
	v_mfma_f32_16x16x32_bf16 v[4:7], v[160:163], v[202:205], v[4:7]
	v_mfma_f32_16x16x32_bf16 v[0:3], v[168:171], v[202:205], v[0:3]
	s_setprio 0
	s_barrier
	s_add_i32 s13, s13, 2
	s_add_u32 s18, s18, 0x100
	s_addc_u32 s19, s19, 0
	s_cmp_lt_u32 s13, 12
	s_cbranch_scc1 .LBB0_1506
	v_mbcnt_lo_u32_b32 v252, -1, 0
	v_mbcnt_hi_u32_b32 v252, -1, v252
	s_lshl_b32 s96, s20, 8
	s_add_i32 s96, s96, s21
	v_and_or_b32 v234, v252, 15, s96
	v_ashrrev_i32_e32 v235, 31, v234
	v_lshl_add_u64 v[234:235], v[234:235], 2, s[2:3]
	global_load_dword v244, v[234:235], off
	global_load_dword v245, v[234:235], off offset:64
	global_load_dword v246, v[234:235], off offset:128
	global_load_dword v247, v[234:235], off offset:192
	global_load_dword v248, v[234:235], off offset:512
	global_load_dword v249, v[234:235], off offset:576
	global_load_dword v250, v[234:235], off offset:640
	global_load_dword v251, v[234:235], off offset:704
	ds_read_b128 v[136:139], v132
	ds_read_b128 v[144:147], v132 offset:1024
	ds_read_b128 v[148:151], v132 offset:2048
	ds_read_b128 v[152:155], v132 offset:3072
	ds_read_b128 v[156:159], v133
	ds_read_b128 v[160:163], v133 offset:1024
	ds_read_b128 v[164:167], v133 offset:2048
	ds_read_b128 v[168:171], v133 offset:3072
	s_ashr_i32 s15, s14, 31
	s_lshl_b64 s[18:19], s[14:15], 19
	s_add_u32 s18, s36, s18
	s_addc_u32 s19, s37, s19
	s_and_b64 s[4:5], s[4:5], exec
	s_cselect_b32 s24, s18, s22
	s_cselect_b32 s25, s19, s23
	s_add_u32 s4, s24, 0x80
	s_addc_u32 s5, s25, 0
	ds_read_b128 v[172:175], v143
	ds_read_b128 v[176:179], v143 offset:1024
	ds_read_b128 v[180:183], v143 offset:2048
	ds_read_b128 v[184:187], v143 offset:3072
	ds_read_b128 v[188:191], v143 offset:4096
	ds_read_b128 v[194:197], v143 offset:5120
	ds_read_b128 v[198:201], v143 offset:6144
	ds_read_b128 v[202:205], v143 offset:7168
	s_add_u32 s22, s22, 0x40780
	s_addc_u32 s23, s23, 0
	s_mov_b32 m0, s57
	s_nop 0
	global_load_lds_dwordx4 v65, s[22:23]
	s_nop 0
	s_mov_b32 m0, s58
	s_nop 0
	global_load_lds_dwordx4 v140, s[22:23]
	s_waitcnt vmcnt(8)
	s_waitcnt lgkmcnt(0)
	s_barrier
	s_setprio 1
	s_waitcnt lgkmcnt(0)
	v_mfma_f32_16x16x32_bf16 v[128:131], v[136:139], v[172:175], v[128:131]
	v_mfma_f32_16x16x32_bf16 v[124:127], v[148:151], v[172:175], v[124:127]
	s_waitcnt lgkmcnt(3)
	v_mfma_f32_16x16x32_bf16 v[110:113], v[136:139], v[188:191], v[110:113]
	v_mfma_f32_16x16x32_bf16 v[106:109], v[148:151], v[188:191], v[106:109]
	v_mfma_f32_16x16x32_bf16 v[128:131], v[144:147], v[176:179], v[128:131]
	v_mfma_f32_16x16x32_bf16 v[124:127], v[152:155], v[176:179], v[124:127]
	v_mfma_f32_16x16x32_bf16 v[120:123], v[136:139], v[180:183], v[120:123]
	v_mfma_f32_16x16x32_bf16 v[116:119], v[148:151], v[180:183], v[116:119]
	s_waitcnt lgkmcnt(2)
	v_mfma_f32_16x16x32_bf16 v[110:113], v[144:147], v[194:197], v[110:113]
	v_mfma_f32_16x16x32_bf16 v[106:109], v[152:155], v[194:197], v[106:109]
	s_waitcnt lgkmcnt(1)
	v_mfma_f32_16x16x32_bf16 v[102:105], v[136:139], v[198:201], v[102:105]
	v_mfma_f32_16x16x32_bf16 v[98:101], v[148:151], v[198:201], v[98:101]
	v_mfma_f32_16x16x32_bf16 v[206:209], v[144:147], v[184:187], v[120:123]
	v_mfma_f32_16x16x32_bf16 v[210:213], v[152:155], v[184:187], v[116:119]
	s_waitcnt lgkmcnt(0)
	v_mfma_f32_16x16x32_bf16 v[214:217], v[144:147], v[202:205], v[102:105]
	v_mfma_f32_16x16x32_bf16 v[218:221], v[152:155], v[202:205], v[98:101]
	s_setprio 0
	s_setprio 1
	v_mfma_f32_16x16x32_bf16 v[94:97], v[156:159], v[172:175], v[94:97]
	v_mfma_f32_16x16x32_bf16 v[90:93], v[164:167], v[172:175], v[90:93]
	v_mfma_f32_16x16x32_bf16 v[70:73], v[156:159], v[198:201], v[70:73]
	v_mfma_f32_16x16x32_bf16 v[66:69], v[164:167], v[198:201], v[66:69]
	v_mfma_f32_16x16x32_bf16 v[94:97], v[160:163], v[176:179], v[94:97]
	v_mfma_f32_16x16x32_bf16 v[90:93], v[168:171], v[176:179], v[90:93]
	v_mfma_f32_16x16x32_bf16 v[86:89], v[156:159], v[180:183], v[86:89]
	v_mfma_f32_16x16x32_bf16 v[82:85], v[164:167], v[180:183], v[82:85]
	v_mfma_f32_16x16x32_bf16 v[78:81], v[156:159], v[188:191], v[78:81]
	v_mfma_f32_16x16x32_bf16 v[74:77], v[164:167], v[188:191], v[74:77]
	v_mfma_f32_16x16x32_bf16 v[70:73], v[160:163], v[202:205], v[70:73]
	v_mfma_f32_16x16x32_bf16 v[66:69], v[168:171], v[202:205], v[66:69]
	v_mfma_f32_16x16x32_bf16 v[172:175], v[160:163], v[184:187], v[86:89]
	v_mfma_f32_16x16x32_bf16 v[176:179], v[168:171], v[184:187], v[82:85]
	v_mfma_f32_16x16x32_bf16 v[180:183], v[160:163], v[194:197], v[78:81]
	v_mfma_f32_16x16x32_bf16 v[184:187], v[168:171], v[194:197], v[74:77]
	s_setprio 0
	s_barrier
	s_nop 0
	ds_read_b128 v[74:77], v143 offset:16384
	ds_read_b128 v[78:81], v143 offset:17408
	ds_read_b128 v[82:85], v143 offset:18432
	ds_read_b128 v[86:89], v143 offset:19456
	ds_read_b128 v[98:101], v143 offset:20480
	ds_read_b128 v[102:105], v143 offset:21504
	ds_read_b128 v[116:119], v143 offset:22528
	ds_read_b128 v[120:123], v143 offset:23552
	s_mov_b64 exec, s[100:101]
	s_mov_b32 m0, s41
	s_nop 0
	global_load_lds_dwordx4 v114, s[16:17]
	s_mov_b64 exec, -1
	s_add_u32 s22, s16, 0x40000
	s_mov_b64 exec, s[100:101]
	s_mov_b32 m0, s42
	s_nop 0
	global_load_lds_dwordx4 v141, s[16:17]
	s_mov_b64 exec, -1
	s_addc_u32 s23, s17, 0
	s_mov_b64 exec, s[100:101]
	s_mov_b32 m0, s43
	s_nop 0
	global_load_lds_dwordx4 v114, s[22:23]
	s_mov_b64 exec, -1
	s_nop 0
	s_mov_b64 exec, s[100:101]
	s_mov_b32 m0, s44
	s_nop 0
	global_load_lds_dwordx4 v141, s[22:23]
	s_mov_b64 exec, -1
	s_nop 0
	s_mov_b64 exec, s[100:101]
	s_mov_b32 m0, s40
	s_nop 0
	global_load_lds_dwordx4 v65, s[24:25]
	s_mov_b64 exec, -1
	s_nop 0
	s_mov_b64 exec, s[100:101]
	s_mov_b32 m0, s45
	s_nop 0
	global_load_lds_dwordx4 v140, s[24:25]
	s_mov_b64 exec, -1
	s_waitcnt vmcnt(8)
	s_waitcnt lgkmcnt(0)
	s_barrier
	s_setprio 1
	s_waitcnt lgkmcnt(0)
	v_mfma_f32_16x16x32_bf16 v[52:55], v[136:139], v[82:85], v[52:55]
	v_mfma_f32_16x16x32_bf16 v[48:51], v[148:151], v[82:85], v[48:51]
	s_waitcnt lgkmcnt(1)
	v_mfma_f32_16x16x32_bf16 v[36:39], v[136:139], v[116:119], v[36:39]
	v_mfma_f32_16x16x32_bf16 v[32:35], v[148:151], v[116:119], v[32:35]
	v_mfma_f32_16x16x32_bf16 v[60:63], v[136:139], v[74:77], v[60:63]
	v_mfma_f32_16x16x32_bf16 v[56:59], v[148:151], v[74:77], v[56:59]
	v_mfma_f32_16x16x32_bf16 v[52:55], v[144:147], v[86:89], v[52:55]
	v_mfma_f32_16x16x32_bf16 v[48:51], v[152:155], v[86:89], v[48:51]
	v_mfma_f32_16x16x32_bf16 v[44:47], v[136:139], v[98:101], v[44:47]
	v_mfma_f32_16x16x32_bf16 v[40:43], v[148:151], v[98:101], v[40:43]
	s_waitcnt lgkmcnt(0)
	v_mfma_f32_16x16x32_bf16 v[36:39], v[144:147], v[120:123], v[36:39]
	v_mfma_f32_16x16x32_bf16 v[32:35], v[152:155], v[120:123], v[32:35]
	v_mfma_f32_16x16x32_bf16 v[188:191], v[144:147], v[78:81], v[60:63]
	v_mfma_f32_16x16x32_bf16 v[194:197], v[152:155], v[78:81], v[56:59]
	v_mfma_f32_16x16x32_bf16 v[198:201], v[144:147], v[102:105], v[44:47]
	v_mfma_f32_16x16x32_bf16 v[202:205], v[152:155], v[102:105], v[40:43]
	s_setprio 0
	s_setprio 1
	v_mfma_f32_16x16x32_bf16 v[20:23], v[156:159], v[82:85], v[20:23]
	v_mfma_f32_16x16x32_bf16 v[16:19], v[164:167], v[82:85], v[16:19]
	v_mfma_f32_16x16x32_bf16 v[12:15], v[156:159], v[98:101], v[12:15]
	v_mfma_f32_16x16x32_bf16 v[8:11], v[164:167], v[98:101], v[8:11]
	v_mfma_f32_16x16x32_bf16 v[28:31], v[156:159], v[74:77], v[28:31]
	v_mfma_f32_16x16x32_bf16 v[24:27], v[164:167], v[74:77], v[24:27]
	v_mfma_f32_16x16x32_bf16 v[20:23], v[160:163], v[86:89], v[20:23]
	v_mfma_f32_16x16x32_bf16 v[16:19], v[168:171], v[86:89], v[16:19]
	v_mfma_f32_16x16x32_bf16 v[12:15], v[160:163], v[102:105], v[12:15]
	v_mfma_f32_16x16x32_bf16 v[8:11], v[168:171], v[102:105], v[8:11]
	v_mfma_f32_16x16x32_bf16 v[4:7], v[156:159], v[116:119], v[4:7]
	v_mfma_f32_16x16x32_bf16 v[0:3], v[164:167], v[116:119], v[0:3]
	v_mfma_f32_16x16x32_bf16 v[136:139], v[160:163], v[78:81], v[28:31]
	v_mfma_f32_16x16x32_bf16 v[144:147], v[168:171], v[78:81], v[24:27]
	v_mfma_f32_16x16x32_bf16 v[148:151], v[160:163], v[120:123], v[4:7]
	v_mfma_f32_16x16x32_bf16 v[152:155], v[168:171], v[120:123], v[0:3]
	s_setprio 0
	s_barrier
	s_nop 1
	ds_read_b128 v[0:3], v134
	ds_read_b128 v[4:7], v134 offset:1024
	ds_read_b128 v[156:159], v134 offset:2048
	ds_read_b128 v[160:163], v134 offset:3072
	ds_read_b128 v[164:167], v135
	ds_read_b128 v[168:171], v135 offset:1024
	ds_read_b128 v[222:225], v135 offset:2048
	ds_read_b128 v[132:135], v135 offset:3072
	ds_read_b128 v[24:27], v143 offset:32768
	ds_read_b128 v[28:31], v143 offset:33792
	ds_read_b128 v[40:43], v143 offset:34816
	ds_read_b128 v[44:47], v143 offset:35840
	ds_read_b128 v[56:59], v143 offset:36864
	ds_read_b128 v[60:63], v143 offset:37888
	ds_read_b128 v[226:229], v143 offset:38912
	ds_read_b128 v[230:233], v143 offset:39936
	s_add_u32 s22, s24, 0x40000
	s_addc_u32 s23, s25, 0
	s_mov_b64 exec, s[100:101]
	s_mov_b32 m0, s46
	s_nop 0
	global_load_lds_dwordx4 v65, s[22:23]
	s_mov_b64 exec, -1
	s_nop 0
	s_mov_b64 exec, s[100:101]
	s_mov_b32 m0, s47
	s_nop 0
	global_load_lds_dwordx4 v140, s[22:23]
	s_mov_b64 exec, -1
	s_waitcnt vmcnt(8)
	s_waitcnt lgkmcnt(0)
	s_barrier
	s_setprio 1
	s_waitcnt lgkmcnt(0)
	v_mfma_f32_16x16x32_bf16 v[74:77], v[0:3], v[24:27], v[128:131]
	s_waitcnt lgkmcnt(6)
	v_mfma_f32_16x16x32_bf16 v[116:119], v[4:7], v[28:31], v[74:77]
	v_mfma_f32_16x16x32_bf16 v[74:77], v[156:159], v[24:27], v[124:127]
	v_mfma_f32_16x16x32_bf16 v[120:123], v[160:163], v[28:31], v[74:77]
	s_waitcnt lgkmcnt(5)
	v_mfma_f32_16x16x32_bf16 v[74:77], v[0:3], v[40:43], v[206:209]
	s_waitcnt lgkmcnt(4)
	v_mfma_f32_16x16x32_bf16 v[98:101], v[4:7], v[44:47], v[74:77]
	v_mfma_f32_16x16x32_bf16 v[74:77], v[156:159], v[40:43], v[210:213]
	v_mfma_f32_16x16x32_bf16 v[102:105], v[160:163], v[44:47], v[74:77]
	s_waitcnt lgkmcnt(3)
	v_mfma_f32_16x16x32_bf16 v[74:77], v[0:3], v[56:59], v[110:113]
	s_waitcnt lgkmcnt(2)
	v_mfma_f32_16x16x32_bf16 v[82:85], v[4:7], v[60:63], v[74:77]
	v_mfma_f32_16x16x32_bf16 v[74:77], v[156:159], v[56:59], v[106:109]
	v_mfma_f32_16x16x32_bf16 v[86:89], v[160:163], v[60:63], v[74:77]
	s_waitcnt lgkmcnt(1)
	v_mfma_f32_16x16x32_bf16 v[74:77], v[0:3], v[226:229], v[214:217]
	s_waitcnt lgkmcnt(0)
	v_mfma_f32_16x16x32_bf16 v[78:81], v[4:7], v[230:233], v[74:77]
	v_mfma_f32_16x16x32_bf16 v[74:77], v[156:159], v[226:229], v[218:221]
	v_mfma_f32_16x16x32_bf16 v[74:77], v[160:163], v[230:233], v[74:77]
	s_setprio 0
	s_setprio 1
	v_mfma_f32_16x16x32_bf16 v[94:97], v[164:167], v[24:27], v[94:97]
	v_mfma_f32_16x16x32_bf16 v[24:27], v[222:225], v[24:27], v[90:93]
	v_mfma_f32_16x16x32_bf16 v[128:131], v[132:135], v[28:31], v[24:27]
	v_mfma_f32_16x16x32_bf16 v[24:27], v[164:167], v[40:43], v[172:175]
	v_mfma_f32_16x16x32_bf16 v[106:109], v[168:171], v[44:47], v[24:27]
	v_mfma_f32_16x16x32_bf16 v[24:27], v[222:225], v[40:43], v[176:179]
	v_mfma_f32_16x16x32_bf16 v[110:113], v[132:135], v[44:47], v[24:27]
	v_mfma_f32_16x16x32_bf16 v[24:27], v[164:167], v[56:59], v[180:183]
	v_mfma_f32_16x16x32_bf16 v[90:93], v[168:171], v[60:63], v[24:27]
	v_mfma_f32_16x16x32_bf16 v[24:27], v[222:225], v[56:59], v[184:187]
	v_mfma_f32_16x16x32_bf16 v[124:127], v[168:171], v[28:31], v[94:97]
	v_mfma_f32_16x16x32_bf16 v[94:97], v[132:135], v[60:63], v[24:27]
	v_mfma_f32_16x16x32_bf16 v[24:27], v[164:167], v[226:229], v[70:73]
	v_mfma_f32_16x16x32_bf16 v[60:63], v[168:171], v[230:233], v[24:27]
	v_mfma_f32_16x16x32_bf16 v[24:27], v[222:225], v[226:229], v[66:69]
	v_mfma_f32_16x16x32_bf16 v[56:59], v[132:135], v[230:233], v[24:27]
	s_setprio 0
	s_barrier
	ds_read_b128 v[172:175], v143 offset:49152
	ds_read_b128 v[176:179], v143 offset:50176
	ds_read_b128 v[180:183], v143 offset:51200
	ds_read_b128 v[184:187], v143 offset:52224
	ds_read_b128 v[206:209], v143 offset:53248
	ds_read_b128 v[210:213], v143 offset:54272
	ds_read_b128 v[214:217], v143 offset:55296
	ds_read_b128 v[218:221], v143 offset:56320
	s_add_u32 s22, s16, 0x80
	s_addc_u32 s23, s17, 0
	s_mov_b64 exec, s[100:101]
	s_mov_b32 m0, s51
	s_nop 0
	global_load_lds_dwordx4 v114, s[22:23]
	s_mov_b64 exec, -1
	s_nop 0
	s_mov_b64 exec, s[100:101]
	s_mov_b32 m0, s52
	s_nop 0
	global_load_lds_dwordx4 v141, s[22:23]
	s_mov_b64 exec, -1
	s_add_u32 s22, s16, 0x40080
	s_addc_u32 s23, s17, 0
	s_mov_b64 exec, s[100:101]
	s_mov_b32 m0, s55
	s_nop 0
	global_load_lds_dwordx4 v114, s[22:23]
	s_mov_b64 exec, -1
	s_nop 0
	s_mov_b64 exec, s[100:101]
	s_mov_b32 m0, s56
	s_nop 0
	global_load_lds_dwordx4 v141, s[22:23]
	s_mov_b64 exec, -1
	s_nop 0
	s_mov_b64 exec, s[100:101]
	s_mov_b32 m0, s53
	s_nop 0
	global_load_lds_dwordx4 v65, s[4:5]
	s_mov_b64 exec, -1
	s_nop 0
	s_mov_b64 exec, s[100:101]
	s_mov_b32 m0, s54
	s_nop 0
	global_load_lds_dwordx4 v140, s[4:5]
	s_mov_b64 exec, -1
	s_waitcnt vmcnt(8)
	s_waitcnt lgkmcnt(0)
	s_barrier
	s_setprio 1
	s_waitcnt lgkmcnt(0)
	v_mfma_f32_16x16x32_bf16 v[24:27], v[0:3], v[172:175], v[188:191]
	s_waitcnt lgkmcnt(6)
	v_mfma_f32_16x16x32_bf16 v[66:69], v[4:7], v[176:179], v[24:27]
	v_mfma_f32_16x16x32_bf16 v[24:27], v[156:159], v[172:175], v[194:197]
	v_mfma_f32_16x16x32_bf16 v[70:73], v[160:163], v[176:179], v[24:27]
	s_waitcnt lgkmcnt(5)
	v_mfma_f32_16x16x32_bf16 v[24:27], v[0:3], v[180:183], v[52:55]
	s_waitcnt lgkmcnt(4)
	v_mfma_f32_16x16x32_bf16 v[40:43], v[4:7], v[184:187], v[24:27]
	v_mfma_f32_16x16x32_bf16 v[24:27], v[156:159], v[180:183], v[48:51]
	v_mfma_f32_16x16x32_bf16 v[44:47], v[160:163], v[184:187], v[24:27]
	s_waitcnt lgkmcnt(3)
	v_mfma_f32_16x16x32_bf16 v[24:27], v[0:3], v[206:209], v[198:201]
	s_waitcnt lgkmcnt(1)
	v_mfma_f32_16x16x32_bf16 v[0:3], v[0:3], v[214:217], v[36:39]
	v_mfma_f32_16x16x32_bf16 v[24:27], v[4:7], v[210:213], v[24:27]
	v_mfma_f32_16x16x32_bf16 v[28:31], v[156:159], v[206:209], v[202:205]
	s_waitcnt lgkmcnt(0)
	v_mfma_f32_16x16x32_bf16 v[0:3], v[4:7], v[218:221], v[0:3]
	v_mfma_f32_16x16x32_bf16 v[4:7], v[156:159], v[214:217], v[32:35]
	v_mfma_f32_16x16x32_bf16 v[28:31], v[160:163], v[210:213], v[28:31]
	v_mfma_f32_16x16x32_bf16 v[4:7], v[160:163], v[218:221], v[4:7]
	s_setprio 0
	s_setprio 1
	v_mfma_f32_16x16x32_bf16 v[32:35], v[164:167], v[172:175], v[136:139]
	v_mfma_f32_16x16x32_bf16 v[52:55], v[168:171], v[176:179], v[32:35]
	v_mfma_f32_16x16x32_bf16 v[32:35], v[222:225], v[172:175], v[144:147]
	v_mfma_f32_16x16x32_bf16 v[20:23], v[164:167], v[180:183], v[20:23]
	v_mfma_f32_16x16x32_bf16 v[16:19], v[222:225], v[180:183], v[16:19]
	v_mfma_f32_16x16x32_bf16 v[12:15], v[164:167], v[206:209], v[12:15]
	v_mfma_f32_16x16x32_bf16 v[8:11], v[222:225], v[206:209], v[8:11]
	v_mfma_f32_16x16x32_bf16 v[48:51], v[132:135], v[176:179], v[32:35]
	v_mfma_f32_16x16x32_bf16 v[36:39], v[168:171], v[184:187], v[20:23]
	v_mfma_f32_16x16x32_bf16 v[32:35], v[132:135], v[184:187], v[16:19]
	v_mfma_f32_16x16x32_bf16 v[20:23], v[168:171], v[210:213], v[12:15]
	v_mfma_f32_16x16x32_bf16 v[16:19], v[132:135], v[210:213], v[8:11]
	v_mfma_f32_16x16x32_bf16 v[8:11], v[164:167], v[214:217], v[148:151]
	v_mfma_f32_16x16x32_bf16 v[12:15], v[222:225], v[214:217], v[152:155]
	v_mfma_f32_16x16x32_bf16 v[8:11], v[168:171], v[218:221], v[8:11]
	v_mfma_f32_16x16x32_bf16 v[12:15], v[132:135], v[218:221], v[12:15]
	s_setprio 0
	s_barrier
	s_andn2_b64 vcc, exec, s[10:11]
	s_cbranch_vccnz .LBB0_1509
	s_barrier
.LBB0_1509:
	s_lshl_b32 s4, s20, 8
	v_mbcnt_lo_u32_b32 v132, -1, 0
	v_mbcnt_hi_u32_b32 v132, -1, v132
	s_add_i32 s4, s4, s21
	v_and_or_b32 v136, v132, 15, s4
	s_lshl_b32 s4, s60, 8
	v_ashrrev_i32_e32 v132, 1, v132
	s_or_b32 s4, s4, s50
	v_and_b32_e32 v132, -8, v132
	v_add_u32_e32 v132, s4, v132
	v_ashrrev_i32_e32 v137, 31, v136
	v_ashrrev_i32_e32 v133, 31, v132
	v_lshlrev_b64 v[134:135], 11, v[136:137]
	v_lshl_add_u64 v[134:135], s[8:9], 0, v[134:135]
	v_lshlrev_b64 v[138:139], 1, v[132:133]
	v_lshl_add_u64 v[132:133], v[134:135], 0, v[138:139]
	v_lshl_add_u64 v[134:135], v[136:137], 2, s[2:3]
	s_mov_b64 s[4:5], 0x40000
	s_waitcnt vmcnt(16) lgkmcnt(0)
	v_mov_b32_e32 v146, v244
	v_mov_b32_e32 v148, v245
	v_mov_b32_e32 v150, v246
	v_mov_b32_e32 v152, v247
	v_mov_b32_e32 v154, v248
	v_mov_b32_e32 v156, v249
	v_mov_b32_e32 v158, v250
	v_mov_b32_e32 v160, v251
	v_pk_mul_f32 v[118:119], v[118:119], v[146:147] op_sel_hi:[1,0]
	v_pk_mul_f32 v[116:117], v[116:117], v[146:147] op_sel_hi:[1,0]
	v_pk_mul_f32 v[122:123], v[122:123], v[146:147] op_sel_hi:[1,0]
	v_pk_mul_f32 v[120:121], v[120:121], v[146:147] op_sel_hi:[1,0]
	v_cvt_pk_bf16_f32 v116, v116, v117
	v_cvt_pk_bf16_f32 v117, v118, v119
	v_cvt_pk_bf16_f32 v118, v120, v121
	v_cvt_pk_bf16_f32 v119, v122, v123
	global_store_dwordx4 v[132:133], v[116:119], off
	v_pk_mul_f32 v[120:121], v[130:131], v[146:147] op_sel_hi:[1,0]
	v_pk_mul_f32 v[122:123], v[128:129], v[146:147] op_sel_hi:[1,0]
	v_pk_mul_f32 v[118:119], v[126:127], v[146:147] op_sel_hi:[1,0]
	v_pk_mul_f32 v[116:117], v[124:125], v[146:147] op_sel_hi:[1,0]
	s_nop 0
	v_cvt_pk_bf16_f32 v116, v116, v117
	v_cvt_pk_bf16_f32 v117, v118, v119
	v_cvt_pk_bf16_f32 v118, v122, v123
	v_cvt_pk_bf16_f32 v119, v120, v121
	global_store_dwordx4 v[132:133], v[116:119], off offset:256
	s_nop 1
	v_or_b32_e32 v116, 16, v136
	v_ashrrev_i32_e32 v117, 31, v116
	v_lshlrev_b64 v[118:119], 11, v[116:117]
	v_lshl_add_u64 v[116:117], v[116:117], 2, s[2:3]
	s_nop 0
	v_lshl_add_u64 v[118:119], s[8:9], 0, v[118:119]
	v_lshl_add_u64 v[118:119], v[118:119], 0, v[138:139]
	s_nop 0
	v_pk_mul_f32 v[100:101], v[100:101], v[148:149] op_sel_hi:[1,0]
	v_pk_mul_f32 v[98:99], v[98:99], v[148:149] op_sel_hi:[1,0]
	v_pk_mul_f32 v[104:105], v[104:105], v[148:149] op_sel_hi:[1,0]
	v_pk_mul_f32 v[102:103], v[102:103], v[148:149] op_sel_hi:[1,0]
	v_cvt_pk_bf16_f32 v98, v98, v99
	v_cvt_pk_bf16_f32 v99, v100, v101
	v_cvt_pk_bf16_f32 v100, v102, v103
	v_cvt_pk_bf16_f32 v101, v104, v105
	global_store_dwordx4 v[118:119], v[98:101], off
	v_pk_mul_f32 v[102:103], v[112:113], v[148:149] op_sel_hi:[1,0]
	v_pk_mul_f32 v[104:105], v[110:111], v[148:149] op_sel_hi:[1,0]
	v_pk_mul_f32 v[100:101], v[108:109], v[148:149] op_sel_hi:[1,0]
	v_pk_mul_f32 v[98:99], v[106:107], v[148:149] op_sel_hi:[1,0]
	s_nop 0
	v_cvt_pk_bf16_f32 v98, v98, v99
	v_cvt_pk_bf16_f32 v99, v100, v101
	v_cvt_pk_bf16_f32 v100, v104, v105
	v_cvt_pk_bf16_f32 v101, v102, v103
	global_store_dwordx4 v[118:119], v[98:101], off offset:256
	s_nop 1
	v_or_b32_e32 v98, 32, v136
	v_ashrrev_i32_e32 v99, 31, v98
	v_lshlrev_b64 v[100:101], 11, v[98:99]
	v_lshl_add_u64 v[98:99], v[98:99], 2, s[2:3]
	s_nop 0
	v_lshl_add_u64 v[100:101], s[8:9], 0, v[100:101]
	v_lshl_add_u64 v[100:101], v[100:101], 0, v[138:139]
	s_nop 0
	v_pk_mul_f32 v[84:85], v[84:85], v[150:151] op_sel_hi:[1,0]
	v_pk_mul_f32 v[82:83], v[82:83], v[150:151] op_sel_hi:[1,0]
	v_pk_mul_f32 v[88:89], v[88:89], v[150:151] op_sel_hi:[1,0]
	v_pk_mul_f32 v[86:87], v[86:87], v[150:151] op_sel_hi:[1,0]
	v_cvt_pk_bf16_f32 v82, v82, v83
	v_cvt_pk_bf16_f32 v83, v84, v85
	v_cvt_pk_bf16_f32 v84, v86, v87
	v_cvt_pk_bf16_f32 v85, v88, v89
	global_store_dwordx4 v[100:101], v[82:85], off
	v_pk_mul_f32 v[86:87], v[96:97], v[150:151] op_sel_hi:[1,0]
	v_pk_mul_f32 v[88:89], v[94:95], v[150:151] op_sel_hi:[1,0]
	v_pk_mul_f32 v[84:85], v[92:93], v[150:151] op_sel_hi:[1,0]
	v_pk_mul_f32 v[82:83], v[90:91], v[150:151] op_sel_hi:[1,0]
	s_nop 0
	v_cvt_pk_bf16_f32 v82, v82, v83
	v_cvt_pk_bf16_f32 v83, v84, v85
	v_cvt_pk_bf16_f32 v84, v88, v89
	v_cvt_pk_bf16_f32 v85, v86, v87
	global_store_dwordx4 v[100:101], v[82:85], off offset:256
	s_nop 1
	v_or_b32_e32 v82, 48, v136
	v_ashrrev_i32_e32 v83, 31, v82
	v_lshlrev_b64 v[84:85], 11, v[82:83]
	v_lshl_add_u64 v[82:83], v[82:83], 2, s[2:3]
	s_nop 0
	v_lshl_add_u64 v[84:85], s[8:9], 0, v[84:85]
	v_lshl_add_u64 v[84:85], v[84:85], 0, v[138:139]
	s_nop 0
	v_pk_mul_f32 v[80:81], v[80:81], v[152:153] op_sel_hi:[1,0]
	v_pk_mul_f32 v[78:79], v[78:79], v[152:153] op_sel_hi:[1,0]
	v_pk_mul_f32 v[86:87], v[76:77], v[152:153] op_sel_hi:[1,0]
	v_pk_mul_f32 v[76:77], v[74:75], v[152:153] op_sel_hi:[1,0]
	v_cvt_pk_bf16_f32 v74, v78, v79
	v_cvt_pk_bf16_f32 v75, v80, v81
	v_cvt_pk_bf16_f32 v76, v76, v77
	v_cvt_pk_bf16_f32 v77, v86, v87
	global_store_dwordx4 v[84:85], v[74:77], off
	v_pk_mul_f32 v[62:63], v[62:63], v[152:153] op_sel_hi:[1,0]
	v_pk_mul_f32 v[60:61], v[60:61], v[152:153] op_sel_hi:[1,0]
	v_pk_mul_f32 v[74:75], v[58:59], v[152:153] op_sel_hi:[1,0]
	v_pk_mul_f32 v[58:59], v[56:57], v[152:153] op_sel_hi:[1,0]
	v_cvt_pk_bf16_f32 v56, v60, v61
	v_cvt_pk_bf16_f32 v57, v62, v63
	v_cvt_pk_bf16_f32 v58, v58, v59
	v_cvt_pk_bf16_f32 v59, v74, v75
	global_store_dwordx4 v[84:85], v[56:59], off offset:256
	s_nop 0
	v_lshl_add_u64 v[60:61], v[132:133], 0, s[4:5]
	s_mov_b32 s4, 0x40000
	s_nop 0
	v_pk_mul_f32 v[58:59], v[68:69], v[154:155] op_sel_hi:[1,0]
	v_pk_mul_f32 v[56:57], v[66:67], v[154:155] op_sel_hi:[1,0]
	v_pk_mul_f32 v[66:67], v[72:73], v[154:155] op_sel_hi:[1,0]
	v_pk_mul_f32 v[68:69], v[70:71], v[154:155] op_sel_hi:[1,0]
	v_cvt_pk_bf16_f32 v56, v56, v57
	v_cvt_pk_bf16_f32 v57, v58, v59
	v_cvt_pk_bf16_f32 v59, v66, v67
	v_add_co_u32_e32 v66, vcc, s4, v132
	v_cvt_pk_bf16_f32 v58, v68, v69
	s_nop 0
	v_addc_co_u32_e32 v67, vcc, 0, v133, vcc
	global_store_dwordx4 v[66:67], v[56:59], off
	v_pk_mul_f32 v[54:55], v[54:55], v[154:155] op_sel_hi:[1,0]
	v_pk_mul_f32 v[52:53], v[52:53], v[154:155] op_sel_hi:[1,0]
	v_pk_mul_f32 v[56:57], v[50:51], v[154:155] op_sel_hi:[1,0]
	v_pk_mul_f32 v[50:51], v[48:49], v[154:155] op_sel_hi:[1,0]
	v_cvt_pk_bf16_f32 v48, v52, v53
	v_cvt_pk_bf16_f32 v49, v54, v55
	v_cvt_pk_bf16_f32 v50, v50, v51
	v_cvt_pk_bf16_f32 v51, v56, v57
	global_store_dwordx4 v[60:61], v[48:51], off offset:256
	s_nop 0
	s_mov_b64 s[4:5], 0x48000
	v_lshl_add_u64 v[48:49], v[132:133], 0, s[4:5]
	s_mov_b32 s4, 0x48000
	s_nop 0
	v_pk_mul_f32 v[42:43], v[42:43], v[156:157] op_sel_hi:[1,0]
	v_pk_mul_f32 v[40:41], v[40:41], v[156:157] op_sel_hi:[1,0]
	v_pk_mul_f32 v[44:45], v[44:45], v[156:157] op_sel_hi:[1,0]
	v_pk_mul_f32 v[46:47], v[46:47], v[156:157] op_sel_hi:[1,0]
	v_cvt_pk_bf16_f32 v40, v40, v41
	v_cvt_pk_bf16_f32 v41, v42, v43
	v_cvt_pk_bf16_f32 v42, v44, v45
	v_add_co_u32_e32 v44, vcc, s4, v132
	v_cvt_pk_bf16_f32 v43, v46, v47
	s_nop 0
	v_addc_co_u32_e32 v45, vcc, 0, v133, vcc
	global_store_dwordx4 v[44:45], v[40:43], off
	v_pk_mul_f32 v[38:39], v[38:39], v[156:157] op_sel_hi:[1,0]
	v_pk_mul_f32 v[36:37], v[36:37], v[156:157] op_sel_hi:[1,0]
	v_pk_mul_f32 v[40:41], v[34:35], v[156:157] op_sel_hi:[1,0]
	v_pk_mul_f32 v[34:35], v[32:33], v[156:157] op_sel_hi:[1,0]
	v_cvt_pk_bf16_f32 v32, v36, v37
	v_cvt_pk_bf16_f32 v33, v38, v39
	v_cvt_pk_bf16_f32 v34, v34, v35
	v_cvt_pk_bf16_f32 v35, v40, v41
	global_store_dwordx4 v[48:49], v[32:35], off offset:256
	s_nop 0
	s_mov_b64 s[4:5], 0x50000
	v_lshl_add_u64 v[32:33], v[132:133], 0, s[4:5]
	s_mov_b32 s4, 0x50000
	s_nop 0
	v_pk_mul_f32 v[26:27], v[26:27], v[158:159] op_sel_hi:[1,0]
	v_pk_mul_f32 v[24:25], v[24:25], v[158:159] op_sel_hi:[1,0]
	v_pk_mul_f32 v[28:29], v[28:29], v[158:159] op_sel_hi:[1,0]
	v_pk_mul_f32 v[30:31], v[30:31], v[158:159] op_sel_hi:[1,0]
	v_cvt_pk_bf16_f32 v24, v24, v25
	v_cvt_pk_bf16_f32 v25, v26, v27
	v_cvt_pk_bf16_f32 v26, v28, v29
	v_add_co_u32_e32 v28, vcc, s4, v132
	v_cvt_pk_bf16_f32 v27, v30, v31
	s_nop 0
	v_addc_co_u32_e32 v29, vcc, 0, v133, vcc
	global_store_dwordx4 v[28:29], v[24:27], off
	v_pk_mul_f32 v[22:23], v[22:23], v[158:159] op_sel_hi:[1,0]
	v_pk_mul_f32 v[20:21], v[20:21], v[158:159] op_sel_hi:[1,0]
	v_pk_mul_f32 v[24:25], v[18:19], v[158:159] op_sel_hi:[1,0]
	v_pk_mul_f32 v[18:19], v[16:17], v[158:159] op_sel_hi:[1,0]
	v_cvt_pk_bf16_f32 v16, v20, v21
	v_cvt_pk_bf16_f32 v17, v22, v23
	v_cvt_pk_bf16_f32 v18, v18, v19
	v_cvt_pk_bf16_f32 v19, v24, v25
	global_store_dwordx4 v[32:33], v[16:19], off offset:256
	s_nop 0
	s_mov_b64 s[4:5], 0x58000
	v_lshl_add_u64 v[18:19], v[132:133], 0, s[4:5]
	s_mov_b32 s4, 0x58000
	s_nop 0
	v_pk_mul_f32 v[2:3], v[2:3], v[160:161] op_sel_hi:[1,0]
	v_pk_mul_f32 v[0:1], v[0:1], v[160:161] op_sel_hi:[1,0]
	v_pk_mul_f32 v[4:5], v[4:5], v[160:161] op_sel_hi:[1,0]
	v_pk_mul_f32 v[6:7], v[6:7], v[160:161] op_sel_hi:[1,0]
	v_cvt_pk_bf16_f32 v0, v0, v1
	v_cvt_pk_bf16_f32 v1, v2, v3
	v_cvt_pk_bf16_f32 v2, v4, v5
	v_add_co_u32_e32 v4, vcc, s4, v132
	v_cvt_pk_bf16_f32 v3, v6, v7
	s_nop 0
	v_addc_co_u32_e32 v5, vcc, 0, v133, vcc
	global_store_dwordx4 v[4:5], v[0:3], off
	v_pk_mul_f32 v[4:5], v[14:15], v[160:161] op_sel_hi:[1,0]
	v_pk_mul_f32 v[6:7], v[12:13], v[160:161] op_sel_hi:[1,0]
	v_pk_mul_f32 v[2:3], v[10:11], v[160:161] op_sel_hi:[1,0]
	v_pk_mul_f32 v[0:1], v[8:9], v[160:161] op_sel_hi:[1,0]
	s_mov_b64 s[4:5], -1
	v_cvt_pk_bf16_f32 v0, v0, v1
	v_cvt_pk_bf16_f32 v1, v2, v3
	v_cvt_pk_bf16_f32 v2, v6, v7
	v_cvt_pk_bf16_f32 v3, v4, v5
	s_and_b64 vcc, exec, s[0:1]
	global_store_dwordx4 v[18:19], v[0:3], off offset:256
	s_cbranch_vccnz .LBB0_1500
	s_andn2_b64 vcc, exec, s[6:7]
	s_cbranch_vccnz .LBB0_1499
	s_barrier
	s_branch .LBB0_1499
